# speedup vs baseline: 1.0099x; 1.0073x over previous
_Z11gemm_kernelPKfPKDF16bS0_Pf:
	s_and_b32 s3, s2, 7
	s_ashr_i32 s14, s2, 3
	s_lshl_b32 s12, s3, 6
	s_load_dwordx8 s[4:11], s[0:1], 0x0
	s_add_i32 s12, s12, s14
	s_bfe_u32 s18, s2, 0x10002
	s_lshl_b32 s2, s12, 6
	s_lshl_b32 s13, s18, 14
	s_and_b32 s2, s2, 0x3f00
	v_lshrrev_b32_e32 v52, 6, v0
	v_and_b32_e32 v50, 15, v0
	v_bfe_u32 v51, v0, 4, 2
	v_bfe_u32 v1, v0, 3, 3
	s_or_b32 s2, s2, s13
	v_lshl_or_b32 v102, v52, 2, v51
	v_lshl_or_b32 v104, v52, 3, v1
	v_lshlrev_b32_e32 v1, 4, v50
	s_lshl_b32 s15, s2, 9
	s_waitcnt lgkmcnt(0)
	s_mov_b32 s28, s10
	s_and_b32 s29, s11, 0xffff
	s_mov_b32 s30, 0x7fffffff
	s_mov_b32 s31, 0x20000
	v_and_b32_e32 v238, 3, v52
	v_lshlrev_b32_e32 v238, 6, v238
	v_lshl_or_b32 v238, v51, 2, v238
	v_lshlrev_b32_e32 v238, 2, v238
	s_and_b32 s24, s12, 3
	s_lshl_b32 s24, s24, 8
	s_lshl_b32 s25, s18, 10
	s_add_u32 s24, s24, s25
	s_lshl_b32 s24, s24, 2
	s_add_u32 s24, s8, s24
	s_addc_u32 s25, s9, 0
	global_load_dwordx4 v[240:243], v238, s[24:25]
	global_load_dwordx4 v[244:247], v238, s[24:25] offset:64
	global_load_dwordx4 v[248:251], v238, s[24:25] offset:128
	global_load_dwordx4 v[252:255], v238, s[24:25] offset:192
	s_mov_b64 s[0:1], s[6:7]
	s_and_b32 s5, s5, 0xffff
	s_mov_b32 s7, 0x20000
	s_brev_b32 s6, -2
	v_lshl_or_b32 v1, v102, 9, v1
	s_or_b32 s2, s15, 0x4000
	s_lshl_b32 s14, s14, 8
	v_lshlrev_b32_e32 v103, 3, v0
	buffer_load_dwordx4 v[54:57], v1, s[4:7], s15 offen sc0 nt
	buffer_load_dwordx4 v[58:61], v1, s[4:7], s2 offen sc0 nt
	s_or_b32 s2, s15, 0x8000
	s_or_b32 s3, s15, 0xc000
	s_lshl_b32 s19, s18, 10
	s_and_b32 s20, s14, 0x300
	v_and_b32_e32 v105, 56, v103
	buffer_load_dwordx4 v[62:65], v1, s[4:7], s2 offen sc0 nt
	buffer_load_dwordx4 v[66:69], v1, s[4:7], s3 offen sc0 nt
	s_or_b32 s2, s15, 0x10000
	s_or_b32 s3, s15, 0x14000
	s_or_b32 s14, s19, s20
	v_lshlrev_b32_e32 v106, 1, v105
	buffer_load_dwordx4 v[70:73], v1, s[4:7], s2 offen sc0 nt
	buffer_load_dwordx4 v[74:77], v1, s[4:7], s3 offen sc0 nt
	s_or_b32 s2, s15, 0x18000
	s_or_b32 s3, s15, 0x1c000
	s_lshl_b32 s14, s14, 11
	buffer_load_dwordx4 v[78:81], v1, s[4:7], s2 offen sc0 nt
	buffer_load_dwordx4 v[82:85], v1, s[4:7], s3 offen sc0 nt
	s_and_b32 s1, s1, 0xffff
	s_mov_b32 s2, s6
	s_mov_b32 s3, s7
	v_lshl_or_b32 v188, v104, 7, v106
	s_or_b32 s16, s14, 0x2000
	buffer_load_dwordx4 v[86:89], v188, s[0:3], s14 offen sc1
	buffer_load_dwordx4 v[90:93], v188, s[0:3], s16 offen sc1
	s_or_b32 s16, s14, 0x4000
	s_or_b32 s17, s14, 0x6000
	buffer_load_dwordx4 v[94:97], v188, s[0:3], s16 offen sc1
	buffer_load_dwordx4 v[98:101], v188, s[0:3], s17 offen sc1
	s_or_b32 s16, s15, 0x100
	s_or_b32 s17, s15, 0x4100
	buffer_load_dwordx4 v[10:13], v1, s[4:7], s16 offen sc0 nt
	buffer_load_dwordx4 v[18:21], v1, s[4:7], s17 offen sc0 nt
	s_or_b32 s16, s15, 0x8100
	s_or_b32 s17, s15, 0xc100
	buffer_load_dwordx4 v[22:25], v1, s[4:7], s16 offen sc0 nt
	buffer_load_dwordx4 v[30:33], v1, s[4:7], s17 offen sc0 nt
	s_or_b32 s16, s15, 0x10100
	s_or_b32 s17, s15, 0x14100
	buffer_load_dwordx4 v[34:37], v1, s[4:7], s16 offen sc0 nt
	buffer_load_dwordx4 v[38:41], v1, s[4:7], s17 offen sc0 nt
	s_or_b32 s16, s15, 0x18100
	s_or_b32 s15, s15, 0x1c100
	buffer_load_dwordx4 v[42:45], v1, s[4:7], s16 offen sc0 nt
	buffer_load_dwordx4 v[46:49], v1, s[4:7], s15 offen sc0 nt
	s_or_b32 s15, s14, 0x8000
	s_or_b32 s16, s14, 0xa000
	buffer_load_dwordx4 v[2:5], v188, s[0:3], s15 offen sc1
	buffer_load_dwordx4 v[6:9], v188, s[0:3], s16 offen sc1
	s_or_b32 s15, s14, 0xc000
	s_or_b32 s16, s14, 0xe000
	buffer_load_dwordx4 v[14:17], v188, s[0:3], s15 offen sc1
	buffer_load_dwordx4 v[26:29], v188, s[0:3], s16 offen sc1
	v_lshrrev_b32_e32 v107, 7, v0
	v_bfe_u32 v108, v0, 3, 1
	v_lshlrev_b32_e32 v102, 6, v102
	s_movk_i32 s2, 0x3c0
	v_and_or_b32 v102, v102, s2, v105
	v_lshrrev_b32_e32 v105, 2, v0
	v_and_or_b32 v107, v107, 2, v108
	v_and_b32_e32 v105, 32, v105
	v_lshlrev_b32_e32 v107, 10, v107
	v_bfe_u32 v103, v103, 5, 1
	v_lshlrev_b32_e32 v104, 6, v104
	v_and_b32_e32 v106, 48, v106
	v_bitop3_b32 v189, v102, v107, v105 bitop3:0xde
	v_bfe_u32 v183, v0, 3, 1
	v_lshlrev_b32_e32 v183, 6, v183
	v_xor_b32_e32 v189, v189, v183
	v_and_or_b32 v103, v52, 6, v103
	v_and_or_b32 v104, v104, s2, v106
	v_lshrrev_b32_e32 v106, 1, v0
	v_lshlrev_b32_e32 v103, 10, v103
	v_and_b32_e32 v106, 32, v106
	v_bitop3_b32 v190, v104, v103, v106 bitop3:0xde
	v_lshrrev_b32_e32 v53, 8, v0
	s_movk_i32 s15, 0x4000
	s_mov_b32 s16, 0x8000
	s_mov_b32 s17, 0xc000
	s_waitcnt vmcnt(23)
	v_cvt_pk_bf16_f32 v57, v56, v57
	v_cvt_pk_bf16_f32 v56, v54, v55
	s_waitcnt vmcnt(22)
	v_cvt_pk_bf16_f32 v55, v60, v61
	v_cvt_pk_bf16_f32 v54, v58, v59
	ds_write2st64_b64 v189, v[56:57], v[54:55] offset1:8
	s_waitcnt vmcnt(21)
	v_cvt_pk_bf16_f32 v55, v64, v65
	v_cvt_pk_bf16_f32 v54, v62, v63
	s_waitcnt vmcnt(20)
	v_cvt_pk_bf16_f32 v57, v68, v69
	v_cvt_pk_bf16_f32 v56, v66, v67
	ds_write2st64_b64 v189, v[54:55], v[56:57] offset0:16 offset1:24
	s_waitcnt vmcnt(19)
	v_cvt_pk_bf16_f32 v55, v72, v73
	v_cvt_pk_bf16_f32 v54, v70, v71
	s_waitcnt vmcnt(18)
	v_cvt_pk_bf16_f32 v57, v76, v77
	v_cvt_pk_bf16_f32 v56, v74, v75
	ds_write2st64_b64 v189, v[54:55], v[56:57] offset0:32 offset1:40
	s_waitcnt vmcnt(17)
	v_cvt_pk_bf16_f32 v55, v80, v81
	v_cvt_pk_bf16_f32 v54, v78, v79
	s_waitcnt vmcnt(16)
	v_cvt_pk_bf16_f32 v57, v84, v85
	v_cvt_pk_bf16_f32 v56, v82, v83
	ds_write2st64_b64 v189, v[54:55], v[56:57] offset0:48 offset1:56
	s_waitcnt vmcnt(15)
	ds_write_b128 v190, v[86:89] offset:32768
	s_waitcnt vmcnt(14)
	ds_write_b128 v190, v[90:93] offset:40960
	s_waitcnt vmcnt(13)
	ds_write_b128 v190, v[94:97] offset:49152
	s_waitcnt vmcnt(12)
	ds_write_b128 v190, v[98:101] offset:57344
	s_waitcnt lgkmcnt(0)
	s_barrier
	v_cmp_eq_u32_e32 vcc, 1, v53
	s_and_saveexec_b64 s[2:3], vcc
	s_cbranch_execz .LBB1_2
	s_barrier

.LBB1_4:
	v_add_u32_e32 v182, s19, v191
	v_add_u32_e32 v238, s19, v192
	v_xor_b32_e32 v185, 64, v238
	ds_read_b128 v[178:181], v182 offset:32768
	ds_read_b128 v[194:197], v182 offset:34816
	ds_read_b128 v[198:201], v182 offset:36864
	ds_read_b128 v[202:205], v182 offset:38912
	ds_read_b128 v[206:209], v238
	ds_read_b128 v[210:213], v238 offset:2048
	ds_read_b128 v[214:217], v238 offset:4096
	ds_read_b128 v[218:221], v238 offset:6144
	ds_read_b128 v[222:225], v238 offset:8192
	ds_read_b128 v[226:229], v238 offset:10240
	ds_read_b128 v[230:233], v238 offset:12288
	ds_read_b128 v[234:237], v238 offset:14336
	s_min_u32 s21, s20, 29
	s_xor_b32 s19, s19, 0x10000
	v_add_u32_e32 v239, s19, v189
	s_waitcnt vmcnt(11)
	v_cvt_pk_bf16_f32 v13, v12, v13
	v_cvt_pk_bf16_f32 v12, v10, v11
	s_waitcnt vmcnt(10)
	v_cvt_pk_bf16_f32 v11, v20, v21
	v_cvt_pk_bf16_f32 v10, v18, v19
	ds_write2st64_b64 v239, v[12:13], v[10:11] offset1:8
	s_waitcnt vmcnt(9)
	v_cvt_pk_bf16_f32 v11, v24, v25
	v_cvt_pk_bf16_f32 v10, v22, v23
	s_waitcnt vmcnt(8)
	v_cvt_pk_bf16_f32 v13, v32, v33
	v_cvt_pk_bf16_f32 v12, v30, v31
	ds_write2st64_b64 v239, v[10:11], v[12:13] offset0:16 offset1:24
	s_waitcnt vmcnt(7)
	v_cvt_pk_bf16_f32 v11, v36, v37
	v_cvt_pk_bf16_f32 v10, v34, v35
	s_waitcnt vmcnt(6)
	v_cvt_pk_bf16_f32 v13, v40, v41
	v_cvt_pk_bf16_f32 v12, v38, v39
	ds_write2st64_b64 v239, v[10:11], v[12:13] offset0:32 offset1:40
	s_waitcnt vmcnt(5)
	v_cvt_pk_bf16_f32 v11, v44, v45
	v_cvt_pk_bf16_f32 v10, v42, v43
	s_waitcnt vmcnt(4)
	v_cvt_pk_bf16_f32 v13, v48, v49
	v_cvt_pk_bf16_f32 v12, v46, v47
	ds_write2st64_b64 v239, v[10:11], v[12:13] offset0:48 offset1:56
	s_waitcnt lgkmcnt(0)
	s_add_i32 s21, s21, 2
	s_barrier
	v_mfma_f32_16x16x32_bf16 v[174:177], v[178:181], v[206:209], v[174:177]
	s_lshl_b32 s22, s21, 1
	s_and_b32 s22, s22, 0x60
	s_add_i32 s22, s22, s12
	s_lshl_b32 s22, s22, 6
	v_mfma_f32_16x16x32_bf16 v[170:173], v[194:197], v[206:209], v[170:173]
	s_and_b32 s22, s22, 0x3f00
	s_or_b32 s22, s22, s13
	s_lshl_b32 s23, s21, 23
	s_lshl_b32 s22, s22, 9
	v_mfma_f32_16x16x32_bf16 v[158:161], v[198:201], v[206:209], v[158:161]
	s_and_b32 s23, s23, 0x7000000
	s_or_b32 s22, s22, s23
	s_lshl_b32 s23, s21, 8
	s_and_b32 s23, s23, 0x100
	s_or_b32 s22, s22, s23
	s_or_b32 s23, s22, 0x4000
	buffer_load_dwordx4 v[10:13], v1, s[4:7], s22 offen sc0 nt
	v_mfma_f32_16x16x32_bf16 v[142:145], v[202:205], v[206:209], v[142:145]
	v_mfma_f32_16x16x32_bf16 v[166:169], v[178:181], v[210:213], v[166:169]
	v_mfma_f32_16x16x32_bf16 v[162:165], v[194:197], v[210:213], v[162:165]
	v_mfma_f32_16x16x32_bf16 v[146:149], v[198:201], v[210:213], v[146:149]
	buffer_load_dwordx4 v[18:21], v1, s[4:7], s23 offen sc0 nt
	s_or_b32 s23, s22, 0x8000
	v_mfma_f32_16x16x32_bf16 v[122:125], v[202:205], v[210:213], v[122:125]
	v_mfma_f32_16x16x32_bf16 v[154:157], v[178:181], v[214:217], v[154:157]
	v_mfma_f32_16x16x32_bf16 v[150:153], v[194:197], v[214:217], v[150:153]
	v_mfma_f32_16x16x32_bf16 v[130:133], v[198:201], v[214:217], v[130:133]
	buffer_load_dwordx4 v[22:25], v1, s[4:7], s23 offen sc0 nt
	s_or_b32 s23, s22, 0xc000
	v_mfma_f32_16x16x32_bf16 v[106:109], v[202:205], v[214:217], v[106:109]
	v_mfma_f32_16x16x32_bf16 v[138:141], v[178:181], v[218:221], v[138:141]
	v_mfma_f32_16x16x32_bf16 v[134:137], v[194:197], v[218:221], v[134:137]
	v_mfma_f32_16x16x32_bf16 v[114:117], v[198:201], v[218:221], v[114:117]
	buffer_load_dwordx4 v[30:33], v1, s[4:7], s23 offen sc0 nt
	s_or_b32 s23, s22, 0x10000
	v_mfma_f32_16x16x32_bf16 v[90:93], v[202:205], v[218:221], v[90:93]
	v_mfma_f32_16x16x32_bf16 v[126:129], v[178:181], v[222:225], v[126:129]
	v_mfma_f32_16x16x32_bf16 v[118:121], v[194:197], v[222:225], v[118:121]
	v_mfma_f32_16x16x32_bf16 v[98:101], v[198:201], v[222:225], v[98:101]
	buffer_load_dwordx4 v[34:37], v1, s[4:7], s23 offen sc0 nt
	s_or_b32 s23, s22, 0x14000
	v_mfma_f32_16x16x32_bf16 v[74:77], v[202:205], v[222:225], v[74:77]
	v_mfma_f32_16x16x32_bf16 v[110:113], v[178:181], v[226:229], v[110:113]
	v_mfma_f32_16x16x32_bf16 v[102:105], v[194:197], v[226:229], v[102:105]
	v_mfma_f32_16x16x32_bf16 v[82:85], v[198:201], v[226:229], v[82:85]
	buffer_load_dwordx4 v[38:41], v1, s[4:7], s23 offen sc0 nt
	s_or_b32 s23, s22, 0x18000
	s_or_b32 s22, s22, 0x1c000
	v_mfma_f32_16x16x32_bf16 v[62:65], v[202:205], v[226:229], v[62:65]
	v_mfma_f32_16x16x32_bf16 v[94:97], v[178:181], v[230:233], v[94:97]
	v_mfma_f32_16x16x32_bf16 v[86:89], v[194:197], v[230:233], v[86:89]
	v_mfma_f32_16x16x32_bf16 v[70:73], v[198:201], v[230:233], v[70:73]
	buffer_load_dwordx4 v[42:45], v1, s[4:7], s23 offen sc0 nt
	v_mfma_f32_16x16x32_bf16 v[54:57], v[202:205], v[230:233], v[54:57]
	v_mfma_f32_16x16x32_bf16 v[78:81], v[178:181], v[234:237], v[78:81]
	v_mfma_f32_16x16x32_bf16 v[66:69], v[194:197], v[234:237], v[66:69]
	v_mfma_f32_16x16x32_bf16 v[58:61], v[198:201], v[234:237], v[58:61]
	buffer_load_dwordx4 v[46:49], v1, s[4:7], s22 offen sc0 nt
	v_mfma_f32_16x16x32_bf16 v[50:53], v[202:205], v[234:237], v[50:53]
	s_waitcnt lgkmcnt(0)
	s_barrier
	ds_read_b128 v[178:181], v182 offset:33792
	ds_read_b128 v[194:197], v182 offset:35840
	ds_read_b128 v[198:201], v182 offset:37888
	ds_read_b128 v[202:205], v182 offset:39936
	ds_read_b128 v[206:209], v185 offset:1024
	ds_read_b128 v[210:213], v185 offset:3072
	ds_read_b128 v[214:217], v185 offset:5120
	ds_read_b128 v[218:221], v185 offset:7168
	ds_read_b128 v[222:225], v185 offset:9216
	ds_read_b128 v[226:229], v185 offset:11264
	ds_read_b128 v[230:233], v185 offset:13312
	ds_read_b128 v[234:237], v185 offset:15360
	v_add_u32_e32 v182, s19, v190
	s_waitcnt vmcnt(11)
	ds_write_b128 v182, v[2:5] offset:32768
	s_waitcnt vmcnt(10)
	ds_write_b128 v182, v[6:9] offset:40960
	s_waitcnt vmcnt(9)
	ds_write_b128 v182, v[14:17] offset:49152
	s_waitcnt vmcnt(8)
	ds_write_b128 v182, v[26:29] offset:57344
	s_waitcnt lgkmcnt(0)
	s_barrier
	v_mfma_f32_16x16x32_bf16 v[174:177], v[178:181], v[206:209], v[174:177]
	s_lshl_b32 s21, s21, 15
	s_and_b32 s21, s21, 0x78000
	s_or_b32 s21, s21, s14
	s_or_b32 s22, s21, 0x2000
	v_mfma_f32_16x16x32_bf16 v[170:173], v[194:197], v[206:209], v[170:173]
	v_mfma_f32_16x16x32_bf16 v[158:161], v[198:201], v[206:209], v[158:161]
	v_mfma_f32_16x16x32_bf16 v[142:145], v[202:205], v[206:209], v[142:145]
	v_mfma_f32_16x16x32_bf16 v[166:169], v[178:181], v[210:213], v[166:169]
	v_mfma_f32_16x16x32_bf16 v[162:165], v[194:197], v[210:213], v[162:165]
	buffer_load_dwordx4 v[2:5], v188, s[0:3], s21 offen sc1
	v_mfma_f32_16x16x32_bf16 v[146:149], v[198:201], v[210:213], v[146:149]
	v_mfma_f32_16x16x32_bf16 v[122:125], v[202:205], v[210:213], v[122:125]
	v_mfma_f32_16x16x32_bf16 v[154:157], v[178:181], v[214:217], v[154:157]
	v_mfma_f32_16x16x32_bf16 v[150:153], v[194:197], v[214:217], v[150:153]
	v_mfma_f32_16x16x32_bf16 v[130:133], v[198:201], v[214:217], v[130:133]
	v_mfma_f32_16x16x32_bf16 v[106:109], v[202:205], v[214:217], v[106:109]
	v_mfma_f32_16x16x32_bf16 v[138:141], v[178:181], v[218:221], v[138:141]
	v_mfma_f32_16x16x32_bf16 v[134:137], v[194:197], v[218:221], v[134:137]
	buffer_load_dwordx4 v[6:9], v188, s[0:3], s22 offen sc1
	s_or_b32 s22, s21, 0x4000
	s_or_b32 s21, s21, 0x6000
	v_mfma_f32_16x16x32_bf16 v[114:117], v[198:201], v[218:221], v[114:117]
	v_mfma_f32_16x16x32_bf16 v[90:93], v[202:205], v[218:221], v[90:93]
	v_mfma_f32_16x16x32_bf16 v[126:129], v[178:181], v[222:225], v[126:129]
	v_mfma_f32_16x16x32_bf16 v[118:121], v[194:197], v[222:225], v[118:121]
	v_mfma_f32_16x16x32_bf16 v[98:101], v[198:201], v[222:225], v[98:101]
	v_mfma_f32_16x16x32_bf16 v[74:77], v[202:205], v[222:225], v[74:77]
	v_mfma_f32_16x16x32_bf16 v[110:113], v[178:181], v[226:229], v[110:113]
	v_mfma_f32_16x16x32_bf16 v[102:105], v[194:197], v[226:229], v[102:105]
	buffer_load_dwordx4 v[14:17], v188, s[0:3], s22 offen sc1
	v_mfma_f32_16x16x32_bf16 v[82:85], v[198:201], v[226:229], v[82:85]
	v_mfma_f32_16x16x32_bf16 v[62:65], v[202:205], v[226:229], v[62:65]
	v_mfma_f32_16x16x32_bf16 v[94:97], v[178:181], v[230:233], v[94:97]
	v_mfma_f32_16x16x32_bf16 v[86:89], v[194:197], v[230:233], v[86:89]
	v_mfma_f32_16x16x32_bf16 v[70:73], v[198:201], v[230:233], v[70:73]
	v_mfma_f32_16x16x32_bf16 v[54:57], v[202:205], v[230:233], v[54:57]
	v_mfma_f32_16x16x32_bf16 v[78:81], v[178:181], v[234:237], v[78:81]
	v_mfma_f32_16x16x32_bf16 v[66:69], v[194:197], v[234:237], v[66:69]
	buffer_load_dwordx4 v[26:29], v188, s[0:3], s21 offen sc1
	v_mfma_f32_16x16x32_bf16 v[58:61], v[198:201], v[234:237], v[58:61]
	v_mfma_f32_16x16x32_bf16 v[50:53], v[202:205], v[234:237], v[50:53]
	s_and_b32 s21, s20, 15
	s_cmp_lg_u32 s21, 15
	s_cbranch_scc1 .LBB1_3
	s_and_b32 s21, s18, 32
	s_add_i32 s21, s21, s12
	s_lshl_b32 s21, s21, 6
	s_and_b32 s21, s21, 0x3f00
	v_add_lshl_u32 v182, v193, s21, 9
	v_add_u32_e32 v206, v184, v182
	buffer_store_dwordx4 v[174:177], v206, s[28:31], 0 offen
	buffer_store_dwordx4 v[170:173], v206, s[28:31], 0 offen offset:64
	buffer_store_dwordx4 v[158:161], v206, s[28:31], 0 offen offset:128
	buffer_store_dwordx4 v[142:145], v206, s[28:31], 0 offen offset:192
	buffer_store_dwordx4 v[166:169], v206, s[28:31], s8 offen
	buffer_store_dwordx4 v[162:165], v206, s[28:31], s8 offen offset:64
	buffer_store_dwordx4 v[146:149], v206, s[28:31], s8 offen offset:128
	buffer_store_dwordx4 v[122:125], v206, s[28:31], s8 offen offset:192
	buffer_store_dwordx4 v[154:157], v206, s[28:31], s15 offen
	buffer_store_dwordx4 v[150:153], v206, s[28:31], s15 offen offset:64
	buffer_store_dwordx4 v[130:133], v206, s[28:31], s15 offen offset:128
	buffer_store_dwordx4 v[106:109], v206, s[28:31], s15 offen offset:192
	buffer_store_dwordx4 v[138:141], v206, s[28:31], s9 offen
	buffer_store_dwordx4 v[134:137], v206, s[28:31], s9 offen offset:64
	buffer_store_dwordx4 v[114:117], v206, s[28:31], s9 offen offset:128
	buffer_store_dwordx4 v[90:93], v206, s[28:31], s9 offen offset:192
	buffer_store_dwordx4 v[126:129], v206, s[28:31], s16 offen
	buffer_store_dwordx4 v[118:121], v206, s[28:31], s16 offen offset:64
	buffer_store_dwordx4 v[98:101], v206, s[28:31], s16 offen offset:128
	buffer_store_dwordx4 v[74:77], v206, s[28:31], s16 offen offset:192
	buffer_store_dwordx4 v[110:113], v206, s[28:31], s10 offen
	buffer_store_dwordx4 v[102:105], v206, s[28:31], s10 offen offset:64
	buffer_store_dwordx4 v[82:85], v206, s[28:31], s10 offen offset:128
	buffer_store_dwordx4 v[62:65], v206, s[28:31], s10 offen offset:192
	buffer_store_dwordx4 v[94:97], v206, s[28:31], s17 offen
	buffer_store_dwordx4 v[86:89], v206, s[28:31], s17 offen offset:64
	buffer_store_dwordx4 v[70:73], v206, s[28:31], s17 offen offset:128
	buffer_store_dwordx4 v[54:57], v206, s[28:31], s17 offen offset:192
	buffer_store_dwordx4 v[78:81], v206, s[28:31], s11 offen
	buffer_store_dwordx4 v[66:69], v206, s[28:31], s11 offen offset:64
	buffer_store_dwordx4 v[58:61], v206, s[28:31], s11 offen offset:128
	buffer_store_dwordx4 v[50:53], v206, s[28:31], s11 offen offset:192
.Lpd_tail:
	s_waitcnt lgkmcnt(0)
	s_barrier
	s_add_i32 s20, s20, 1
	s_add_i32 s18, s18, 2
	v_add_u32_e32 v182, s19, v191
	v_add_u32_e32 v238, s19, v192
	v_xor_b32_e32 v185, 64, v238
	ds_read_b128 v[178:181], v182 offset:32768
	ds_read_b128 v[194:197], v182 offset:34816
	ds_read_b128 v[198:201], v182 offset:36864
	ds_read_b128 v[202:205], v182 offset:38912
	ds_read_b128 v[206:209], v238
	ds_read_b128 v[210:213], v238 offset:2048
	ds_read_b128 v[214:217], v238 offset:4096
	ds_read_b128 v[218:221], v238 offset:6144
	ds_read_b128 v[222:225], v238 offset:8192
	ds_read_b128 v[226:229], v238 offset:10240
	ds_read_b128 v[230:233], v238 offset:12288
	ds_read_b128 v[234:237], v238 offset:14336
	s_min_u32 s21, s20, 29
	s_xor_b32 s19, s19, 0x10000
	v_add_u32_e32 v239, s19, v189
	s_waitcnt vmcnt(43)
	v_cvt_pk_bf16_f32 v13, v12, v13
	v_cvt_pk_bf16_f32 v12, v10, v11
	s_waitcnt vmcnt(42)
	v_cvt_pk_bf16_f32 v11, v20, v21
	v_cvt_pk_bf16_f32 v10, v18, v19
	ds_write2st64_b64 v239, v[12:13], v[10:11] offset1:8
	s_waitcnt vmcnt(41)
	v_cvt_pk_bf16_f32 v11, v24, v25
	v_cvt_pk_bf16_f32 v10, v22, v23
	s_waitcnt vmcnt(40)
	v_cvt_pk_bf16_f32 v13, v32, v33
	v_cvt_pk_bf16_f32 v12, v30, v31
	ds_write2st64_b64 v239, v[10:11], v[12:13] offset0:16 offset1:24
	s_waitcnt vmcnt(39)
	v_cvt_pk_bf16_f32 v11, v36, v37
	v_cvt_pk_bf16_f32 v10, v34, v35
	s_waitcnt vmcnt(38)
	v_cvt_pk_bf16_f32 v13, v40, v41
	v_cvt_pk_bf16_f32 v12, v38, v39
	ds_write2st64_b64 v239, v[10:11], v[12:13] offset0:32 offset1:40
	s_waitcnt vmcnt(37)
	v_cvt_pk_bf16_f32 v11, v44, v45
	v_cvt_pk_bf16_f32 v10, v42, v43
	s_waitcnt vmcnt(36)
	v_cvt_pk_bf16_f32 v13, v48, v49
	v_cvt_pk_bf16_f32 v12, v46, v47
	ds_write2st64_b64 v239, v[10:11], v[12:13] offset0:48 offset1:56
	s_waitcnt lgkmcnt(0)
	s_add_i32 s21, s21, 2
	s_barrier
	v_mfma_f32_16x16x32_bf16 v[174:177], v[178:181], v[206:209], v[240:243]
	s_lshl_b32 s22, s21, 1
	s_and_b32 s22, s22, 0x60
	s_add_i32 s22, s22, s12
	s_lshl_b32 s22, s22, 6
	v_mfma_f32_16x16x32_bf16 v[170:173], v[194:197], v[206:209], v[244:247]
	s_and_b32 s22, s22, 0x3f00
	s_or_b32 s22, s22, s13
	s_lshl_b32 s23, s21, 23
	s_lshl_b32 s22, s22, 9
	v_mfma_f32_16x16x32_bf16 v[158:161], v[198:201], v[206:209], v[248:251]
	s_and_b32 s23, s23, 0x7000000
	s_or_b32 s22, s22, s23
	s_lshl_b32 s23, s21, 8
	s_and_b32 s23, s23, 0x100
	s_or_b32 s22, s22, s23
	s_or_b32 s23, s22, 0x4000
	buffer_load_dwordx4 v[10:13], v1, s[4:7], s22 offen sc0 nt
	v_mfma_f32_16x16x32_bf16 v[142:145], v[202:205], v[206:209], v[252:255]
	v_mfma_f32_16x16x32_bf16 v[166:169], v[178:181], v[210:213], v[240:243]
	v_mfma_f32_16x16x32_bf16 v[162:165], v[194:197], v[210:213], v[244:247]
	v_mfma_f32_16x16x32_bf16 v[146:149], v[198:201], v[210:213], v[248:251]
	buffer_load_dwordx4 v[18:21], v1, s[4:7], s23 offen sc0 nt
	s_or_b32 s23, s22, 0x8000
	v_mfma_f32_16x16x32_bf16 v[122:125], v[202:205], v[210:213], v[252:255]
	v_mfma_f32_16x16x32_bf16 v[154:157], v[178:181], v[214:217], v[240:243]
	v_mfma_f32_16x16x32_bf16 v[150:153], v[194:197], v[214:217], v[244:247]
	v_mfma_f32_16x16x32_bf16 v[130:133], v[198:201], v[214:217], v[248:251]
	buffer_load_dwordx4 v[22:25], v1, s[4:7], s23 offen sc0 nt
	s_or_b32 s23, s22, 0xc000
	v_mfma_f32_16x16x32_bf16 v[106:109], v[202:205], v[214:217], v[252:255]
	v_mfma_f32_16x16x32_bf16 v[138:141], v[178:181], v[218:221], v[240:243]
	v_mfma_f32_16x16x32_bf16 v[134:137], v[194:197], v[218:221], v[244:247]
	v_mfma_f32_16x16x32_bf16 v[114:117], v[198:201], v[218:221], v[248:251]
	buffer_load_dwordx4 v[30:33], v1, s[4:7], s23 offen sc0 nt
	s_or_b32 s23, s22, 0x10000
	v_mfma_f32_16x16x32_bf16 v[90:93], v[202:205], v[218:221], v[252:255]
	v_mfma_f32_16x16x32_bf16 v[126:129], v[178:181], v[222:225], v[240:243]
	v_mfma_f32_16x16x32_bf16 v[118:121], v[194:197], v[222:225], v[244:247]
	v_mfma_f32_16x16x32_bf16 v[98:101], v[198:201], v[222:225], v[248:251]
	buffer_load_dwordx4 v[34:37], v1, s[4:7], s23 offen sc0 nt
	s_or_b32 s23, s22, 0x14000
	v_mfma_f32_16x16x32_bf16 v[74:77], v[202:205], v[222:225], v[252:255]
	v_mfma_f32_16x16x32_bf16 v[110:113], v[178:181], v[226:229], v[240:243]
	v_mfma_f32_16x16x32_bf16 v[102:105], v[194:197], v[226:229], v[244:247]
	v_mfma_f32_16x16x32_bf16 v[82:85], v[198:201], v[226:229], v[248:251]
	buffer_load_dwordx4 v[38:41], v1, s[4:7], s23 offen sc0 nt
	s_or_b32 s23, s22, 0x18000
	s_or_b32 s22, s22, 0x1c000
	v_mfma_f32_16x16x32_bf16 v[62:65], v[202:205], v[226:229], v[252:255]
	v_mfma_f32_16x16x32_bf16 v[94:97], v[178:181], v[230:233], v[240:243]
	v_mfma_f32_16x16x32_bf16 v[86:89], v[194:197], v[230:233], v[244:247]
	v_mfma_f32_16x16x32_bf16 v[70:73], v[198:201], v[230:233], v[248:251]
	buffer_load_dwordx4 v[42:45], v1, s[4:7], s23 offen sc0 nt
	v_mfma_f32_16x16x32_bf16 v[54:57], v[202:205], v[230:233], v[252:255]
	v_mfma_f32_16x16x32_bf16 v[78:81], v[178:181], v[234:237], v[240:243]
	v_mfma_f32_16x16x32_bf16 v[66:69], v[194:197], v[234:237], v[244:247]
	v_mfma_f32_16x16x32_bf16 v[58:61], v[198:201], v[234:237], v[248:251]
	buffer_load_dwordx4 v[46:49], v1, s[4:7], s22 offen sc0 nt
	v_mfma_f32_16x16x32_bf16 v[50:53], v[202:205], v[234:237], v[252:255]
	s_waitcnt lgkmcnt(0)
	s_barrier
	ds_read_b128 v[178:181], v182 offset:33792
	ds_read_b128 v[194:197], v182 offset:35840
	ds_read_b128 v[198:201], v182 offset:37888
	ds_read_b128 v[202:205], v182 offset:39936
	ds_read_b128 v[206:209], v185 offset:1024
	ds_read_b128 v[210:213], v185 offset:3072
	ds_read_b128 v[214:217], v185 offset:5120
	ds_read_b128 v[218:221], v185 offset:7168
	ds_read_b128 v[222:225], v185 offset:9216
	ds_read_b128 v[226:229], v185 offset:11264
	ds_read_b128 v[230:233], v185 offset:13312
	ds_read_b128 v[234:237], v185 offset:15360
	v_add_u32_e32 v182, s19, v190
	s_waitcnt vmcnt(43)
	ds_write_b128 v182, v[2:5] offset:32768
	s_waitcnt vmcnt(42)
	ds_write_b128 v182, v[6:9] offset:40960
	s_waitcnt vmcnt(41)
	ds_write_b128 v182, v[14:17] offset:49152
	s_waitcnt vmcnt(40)
	ds_write_b128 v182, v[26:29] offset:57344
	s_waitcnt lgkmcnt(0)
	s_barrier
	v_mfma_f32_16x16x32_bf16 v[174:177], v[178:181], v[206:209], v[174:177]
	s_lshl_b32 s21, s21, 15
	s_and_b32 s21, s21, 0x78000
	s_or_b32 s21, s21, s14
	s_or_b32 s22, s21, 0x2000
	v_mfma_f32_16x16x32_bf16 v[170:173], v[194:197], v[206:209], v[170:173]
	v_mfma_f32_16x16x32_bf16 v[158:161], v[198:201], v[206:209], v[158:161]
	v_mfma_f32_16x16x32_bf16 v[142:145], v[202:205], v[206:209], v[142:145]
	v_mfma_f32_16x16x32_bf16 v[166:169], v[178:181], v[210:213], v[166:169]
	v_mfma_f32_16x16x32_bf16 v[162:165], v[194:197], v[210:213], v[162:165]
	buffer_load_dwordx4 v[2:5], v188, s[0:3], s21 offen sc1
	v_mfma_f32_16x16x32_bf16 v[146:149], v[198:201], v[210:213], v[146:149]
	v_mfma_f32_16x16x32_bf16 v[122:125], v[202:205], v[210:213], v[122:125]
	v_mfma_f32_16x16x32_bf16 v[154:157], v[178:181], v[214:217], v[154:157]
	v_mfma_f32_16x16x32_bf16 v[150:153], v[194:197], v[214:217], v[150:153]
	v_mfma_f32_16x16x32_bf16 v[130:133], v[198:201], v[214:217], v[130:133]
	v_mfma_f32_16x16x32_bf16 v[106:109], v[202:205], v[214:217], v[106:109]
	v_mfma_f32_16x16x32_bf16 v[138:141], v[178:181], v[218:221], v[138:141]
	v_mfma_f32_16x16x32_bf16 v[134:137], v[194:197], v[218:221], v[134:137]
	buffer_load_dwordx4 v[6:9], v188, s[0:3], s22 offen sc1
	s_or_b32 s22, s21, 0x4000
	s_or_b32 s21, s21, 0x6000
	v_mfma_f32_16x16x32_bf16 v[114:117], v[198:201], v[218:221], v[114:117]
	v_mfma_f32_16x16x32_bf16 v[90:93], v[202:205], v[218:221], v[90:93]
	v_mfma_f32_16x16x32_bf16 v[126:129], v[178:181], v[222:225], v[126:129]
	v_mfma_f32_16x16x32_bf16 v[118:121], v[194:197], v[222:225], v[118:121]
	v_mfma_f32_16x16x32_bf16 v[98:101], v[198:201], v[222:225], v[98:101]
	v_mfma_f32_16x16x32_bf16 v[74:77], v[202:205], v[222:225], v[74:77]
	v_mfma_f32_16x16x32_bf16 v[110:113], v[178:181], v[226:229], v[110:113]
	v_mfma_f32_16x16x32_bf16 v[102:105], v[194:197], v[226:229], v[102:105]
	buffer_load_dwordx4 v[14:17], v188, s[0:3], s22 offen sc1
	v_mfma_f32_16x16x32_bf16 v[82:85], v[198:201], v[226:229], v[82:85]
	v_mfma_f32_16x16x32_bf16 v[62:65], v[202:205], v[226:229], v[62:65]
	v_mfma_f32_16x16x32_bf16 v[94:97], v[178:181], v[230:233], v[94:97]
	v_mfma_f32_16x16x32_bf16 v[86:89], v[194:197], v[230:233], v[86:89]
	v_mfma_f32_16x16x32_bf16 v[70:73], v[198:201], v[230:233], v[70:73]
	v_mfma_f32_16x16x32_bf16 v[54:57], v[202:205], v[230:233], v[54:57]
	v_mfma_f32_16x16x32_bf16 v[78:81], v[178:181], v[234:237], v[78:81]
	v_mfma_f32_16x16x32_bf16 v[66:69], v[194:197], v[234:237], v[66:69]
	buffer_load_dwordx4 v[26:29], v188, s[0:3], s21 offen sc1
	v_mfma_f32_16x16x32_bf16 v[58:61], v[198:201], v[234:237], v[58:61]
	v_mfma_f32_16x16x32_bf16 v[50:53], v[202:205], v[234:237], v[50:53]
	s_branch .LBB1_3
.Lt30:
	v_add_u32_e32 v182, s19, v191
	v_add_u32_e32 v238, s19, v192
	v_xor_b32_e32 v185, 64, v238
	ds_read_b128 v[178:181], v182 offset:32768
	ds_read_b128 v[194:197], v182 offset:34816
	ds_read_b128 v[198:201], v182 offset:36864
	ds_read_b128 v[202:205], v182 offset:38912
	ds_read_b128 v[206:209], v238
	ds_read_b128 v[210:213], v238 offset:2048
	ds_read_b128 v[214:217], v238 offset:4096
	ds_read_b128 v[218:221], v238 offset:6144
	ds_read_b128 v[222:225], v238 offset:8192
	ds_read_b128 v[226:229], v238 offset:10240
	ds_read_b128 v[230:233], v238 offset:12288
	ds_read_b128 v[234:237], v238 offset:14336
	s_min_u32 s21, s20, 29
	s_xor_b32 s19, s19, 0x10000
	v_add_u32_e32 v239, s19, v189
	s_waitcnt vmcnt(11)
	v_cvt_pk_bf16_f32 v13, v12, v13
	v_cvt_pk_bf16_f32 v12, v10, v11
	s_waitcnt vmcnt(10)
	v_cvt_pk_bf16_f32 v11, v20, v21
	v_cvt_pk_bf16_f32 v10, v18, v19
	ds_write2st64_b64 v239, v[12:13], v[10:11] offset1:8
	s_waitcnt vmcnt(9)
	v_cvt_pk_bf16_f32 v11, v24, v25
	v_cvt_pk_bf16_f32 v10, v22, v23
	s_waitcnt vmcnt(8)
	v_cvt_pk_bf16_f32 v13, v32, v33
	v_cvt_pk_bf16_f32 v12, v30, v31
	ds_write2st64_b64 v239, v[10:11], v[12:13] offset0:16 offset1:24
	s_waitcnt vmcnt(7)
	v_cvt_pk_bf16_f32 v11, v36, v37
	v_cvt_pk_bf16_f32 v10, v34, v35
	s_waitcnt vmcnt(6)
	v_cvt_pk_bf16_f32 v13, v40, v41
	v_cvt_pk_bf16_f32 v12, v38, v39
	ds_write2st64_b64 v239, v[10:11], v[12:13] offset0:32 offset1:40
	s_waitcnt vmcnt(5)
	v_cvt_pk_bf16_f32 v11, v44, v45
	v_cvt_pk_bf16_f32 v10, v42, v43
	s_waitcnt vmcnt(4)
	v_cvt_pk_bf16_f32 v13, v48, v49
	v_cvt_pk_bf16_f32 v12, v46, v47
	ds_write2st64_b64 v239, v[10:11], v[12:13] offset0:48 offset1:56
	s_waitcnt lgkmcnt(0)
	s_add_i32 s21, s21, 2
	s_barrier
	v_mfma_f32_16x16x32_bf16 v[174:177], v[178:181], v[206:209], v[174:177]
	s_lshl_b32 s22, s21, 1
	s_and_b32 s22, s22, 0x60
	s_add_i32 s22, s22, s12
	s_lshl_b32 s22, s22, 6
	v_mfma_f32_16x16x32_bf16 v[170:173], v[194:197], v[206:209], v[170:173]
	s_and_b32 s22, s22, 0x3f00
	s_or_b32 s22, s22, s13
	s_lshl_b32 s23, s21, 23
	s_lshl_b32 s22, s22, 9
	v_mfma_f32_16x16x32_bf16 v[158:161], v[198:201], v[206:209], v[158:161]
	s_and_b32 s23, s23, 0x7000000
	s_or_b32 s22, s22, s23
	s_lshl_b32 s23, s21, 8
	s_and_b32 s23, s23, 0x100
	s_or_b32 s22, s22, s23
	s_or_b32 s23, s22, 0x4000
	v_mfma_f32_16x16x32_bf16 v[142:145], v[202:205], v[206:209], v[142:145]
	v_mfma_f32_16x16x32_bf16 v[166:169], v[178:181], v[210:213], v[166:169]
	v_mfma_f32_16x16x32_bf16 v[162:165], v[194:197], v[210:213], v[162:165]
	v_mfma_f32_16x16x32_bf16 v[146:149], v[198:201], v[210:213], v[146:149]
	s_or_b32 s23, s22, 0x8000
	v_mfma_f32_16x16x32_bf16 v[122:125], v[202:205], v[210:213], v[122:125]
	v_mfma_f32_16x16x32_bf16 v[154:157], v[178:181], v[214:217], v[154:157]
	v_mfma_f32_16x16x32_bf16 v[150:153], v[194:197], v[214:217], v[150:153]
	v_mfma_f32_16x16x32_bf16 v[130:133], v[198:201], v[214:217], v[130:133]
	s_or_b32 s23, s22, 0xc000
	v_mfma_f32_16x16x32_bf16 v[106:109], v[202:205], v[214:217], v[106:109]
	v_mfma_f32_16x16x32_bf16 v[138:141], v[178:181], v[218:221], v[138:141]
	v_mfma_f32_16x16x32_bf16 v[134:137], v[194:197], v[218:221], v[134:137]
	v_mfma_f32_16x16x32_bf16 v[114:117], v[198:201], v[218:221], v[114:117]
	s_or_b32 s23, s22, 0x10000
	v_mfma_f32_16x16x32_bf16 v[90:93], v[202:205], v[218:221], v[90:93]
	v_mfma_f32_16x16x32_bf16 v[126:129], v[178:181], v[222:225], v[126:129]
	v_mfma_f32_16x16x32_bf16 v[118:121], v[194:197], v[222:225], v[118:121]
	v_mfma_f32_16x16x32_bf16 v[98:101], v[198:201], v[222:225], v[98:101]
	s_or_b32 s23, s22, 0x14000
	v_mfma_f32_16x16x32_bf16 v[74:77], v[202:205], v[222:225], v[74:77]
	v_mfma_f32_16x16x32_bf16 v[110:113], v[178:181], v[226:229], v[110:113]
	v_mfma_f32_16x16x32_bf16 v[102:105], v[194:197], v[226:229], v[102:105]
	v_mfma_f32_16x16x32_bf16 v[82:85], v[198:201], v[226:229], v[82:85]
	s_or_b32 s23, s22, 0x18000
	s_or_b32 s22, s22, 0x1c000
	v_mfma_f32_16x16x32_bf16 v[62:65], v[202:205], v[226:229], v[62:65]
	v_mfma_f32_16x16x32_bf16 v[94:97], v[178:181], v[230:233], v[94:97]
	v_mfma_f32_16x16x32_bf16 v[86:89], v[194:197], v[230:233], v[86:89]
	v_mfma_f32_16x16x32_bf16 v[70:73], v[198:201], v[230:233], v[70:73]
	v_mfma_f32_16x16x32_bf16 v[54:57], v[202:205], v[230:233], v[54:57]
	v_mfma_f32_16x16x32_bf16 v[78:81], v[178:181], v[234:237], v[78:81]
	v_mfma_f32_16x16x32_bf16 v[66:69], v[194:197], v[234:237], v[66:69]
	v_mfma_f32_16x16x32_bf16 v[58:61], v[198:201], v[234:237], v[58:61]
	v_mfma_f32_16x16x32_bf16 v[50:53], v[202:205], v[234:237], v[50:53]
	s_waitcnt lgkmcnt(0)
	s_barrier
	ds_read_b128 v[178:181], v182 offset:33792
	ds_read_b128 v[194:197], v182 offset:35840
	ds_read_b128 v[198:201], v182 offset:37888
	ds_read_b128 v[202:205], v182 offset:39936
	ds_read_b128 v[206:209], v185 offset:1024
	ds_read_b128 v[210:213], v185 offset:3072
	ds_read_b128 v[214:217], v185 offset:5120
	ds_read_b128 v[218:221], v185 offset:7168
	ds_read_b128 v[222:225], v185 offset:9216
	ds_read_b128 v[226:229], v185 offset:11264
	ds_read_b128 v[230:233], v185 offset:13312
	ds_read_b128 v[234:237], v185 offset:15360
	v_add_u32_e32 v182, s19, v190
	s_waitcnt vmcnt(3)
	ds_write_b128 v182, v[2:5] offset:32768
	s_waitcnt vmcnt(2)
	ds_write_b128 v182, v[6:9] offset:40960
	s_waitcnt vmcnt(1)
	ds_write_b128 v182, v[14:17] offset:49152
	s_waitcnt vmcnt(0)
	ds_write_b128 v182, v[26:29] offset:57344
	s_waitcnt lgkmcnt(0)
	s_barrier
	v_mfma_f32_16x16x32_bf16 v[174:177], v[178:181], v[206:209], v[174:177]
	s_lshl_b32 s21, s21, 15
	s_and_b32 s21, s21, 0x78000
	s_or_b32 s21, s21, s14
	s_or_b32 s22, s21, 0x2000
	v_mfma_f32_16x16x32_bf16 v[170:173], v[194:197], v[206:209], v[170:173]
	v_mfma_f32_16x16x32_bf16 v[158:161], v[198:201], v[206:209], v[158:161]
	v_mfma_f32_16x16x32_bf16 v[142:145], v[202:205], v[206:209], v[142:145]
	v_mfma_f32_16x16x32_bf16 v[166:169], v[178:181], v[210:213], v[166:169]
	v_mfma_f32_16x16x32_bf16 v[162:165], v[194:197], v[210:213], v[162:165]
	v_mfma_f32_16x16x32_bf16 v[146:149], v[198:201], v[210:213], v[146:149]
	v_mfma_f32_16x16x32_bf16 v[122:125], v[202:205], v[210:213], v[122:125]
	v_mfma_f32_16x16x32_bf16 v[154:157], v[178:181], v[214:217], v[154:157]
	v_mfma_f32_16x16x32_bf16 v[150:153], v[194:197], v[214:217], v[150:153]
	v_mfma_f32_16x16x32_bf16 v[130:133], v[198:201], v[214:217], v[130:133]
	v_mfma_f32_16x16x32_bf16 v[106:109], v[202:205], v[214:217], v[106:109]
	v_mfma_f32_16x16x32_bf16 v[138:141], v[178:181], v[218:221], v[138:141]
	v_mfma_f32_16x16x32_bf16 v[134:137], v[194:197], v[218:221], v[134:137]
	s_or_b32 s22, s21, 0x4000
	s_or_b32 s21, s21, 0x6000
	v_mfma_f32_16x16x32_bf16 v[114:117], v[198:201], v[218:221], v[114:117]
	v_mfma_f32_16x16x32_bf16 v[90:93], v[202:205], v[218:221], v[90:93]
	v_mfma_f32_16x16x32_bf16 v[126:129], v[178:181], v[222:225], v[126:129]
	v_mfma_f32_16x16x32_bf16 v[118:121], v[194:197], v[222:225], v[118:121]
	v_mfma_f32_16x16x32_bf16 v[98:101], v[198:201], v[222:225], v[98:101]
	v_mfma_f32_16x16x32_bf16 v[74:77], v[202:205], v[222:225], v[74:77]
	v_mfma_f32_16x16x32_bf16 v[110:113], v[178:181], v[226:229], v[110:113]
	v_mfma_f32_16x16x32_bf16 v[102:105], v[194:197], v[226:229], v[102:105]
	v_mfma_f32_16x16x32_bf16 v[82:85], v[198:201], v[226:229], v[82:85]
	v_mfma_f32_16x16x32_bf16 v[62:65], v[202:205], v[226:229], v[62:65]
	v_mfma_f32_16x16x32_bf16 v[94:97], v[178:181], v[230:233], v[94:97]
	v_mfma_f32_16x16x32_bf16 v[86:89], v[194:197], v[230:233], v[86:89]
	v_mfma_f32_16x16x32_bf16 v[70:73], v[198:201], v[230:233], v[70:73]
	v_mfma_f32_16x16x32_bf16 v[54:57], v[202:205], v[230:233], v[54:57]
	v_mfma_f32_16x16x32_bf16 v[78:81], v[178:181], v[234:237], v[78:81]
	v_mfma_f32_16x16x32_bf16 v[66:69], v[194:197], v[234:237], v[66:69]
	v_mfma_f32_16x16x32_bf16 v[58:61], v[198:201], v[234:237], v[58:61]
	v_mfma_f32_16x16x32_bf16 v[50:53], v[202:205], v[234:237], v[50:53]
	s_waitcnt lgkmcnt(0)
	s_barrier
	s_add_i32 s20, s20, 1
	s_add_i32 s18, s18, 2
	v_add_u32_e32 v182, s19, v191
	v_add_u32_e32 v238, s19, v192
	v_xor_b32_e32 v185, 64, v238
	ds_read_b128 v[178:181], v182 offset:32768
	ds_read_b128 v[194:197], v182 offset:34816
	ds_read_b128 v[198:201], v182 offset:36864
	ds_read_b128 v[202:205], v182 offset:38912
	ds_read_b128 v[206:209], v238
	ds_read_b128 v[210:213], v238 offset:2048
	ds_read_b128 v[214:217], v238 offset:4096
	ds_read_b128 v[218:221], v238 offset:6144
	ds_read_b128 v[222:225], v238 offset:8192
	ds_read_b128 v[226:229], v238 offset:10240
	ds_read_b128 v[230:233], v238 offset:12288
	ds_read_b128 v[234:237], v238 offset:14336
	s_min_u32 s21, s20, 29
	s_xor_b32 s19, s19, 0x10000
	v_add_u32_e32 v239, s19, v189
	s_waitcnt lgkmcnt(0)
	s_add_i32 s21, s21, 2
	s_barrier
	v_mfma_f32_16x16x32_bf16 v[174:177], v[178:181], v[206:209], v[174:177]
	s_lshl_b32 s22, s21, 1
	s_and_b32 s22, s22, 0x60
	s_add_i32 s22, s22, s12
	s_lshl_b32 s22, s22, 6
	v_mfma_f32_16x16x32_bf16 v[170:173], v[194:197], v[206:209], v[170:173]
	s_and_b32 s22, s22, 0x3f00
	s_or_b32 s22, s22, s13
	s_lshl_b32 s23, s21, 23
	s_lshl_b32 s22, s22, 9
	v_mfma_f32_16x16x32_bf16 v[158:161], v[198:201], v[206:209], v[158:161]
	s_and_b32 s23, s23, 0x7000000
	s_or_b32 s22, s22, s23
	s_lshl_b32 s23, s21, 8
	s_and_b32 s23, s23, 0x100
	s_or_b32 s22, s22, s23
	s_or_b32 s23, s22, 0x4000
	v_mfma_f32_16x16x32_bf16 v[142:145], v[202:205], v[206:209], v[142:145]
	v_mfma_f32_16x16x32_bf16 v[166:169], v[178:181], v[210:213], v[166:169]
	v_mfma_f32_16x16x32_bf16 v[162:165], v[194:197], v[210:213], v[162:165]
	v_mfma_f32_16x16x32_bf16 v[146:149], v[198:201], v[210:213], v[146:149]
	s_or_b32 s23, s22, 0x8000
	v_mfma_f32_16x16x32_bf16 v[122:125], v[202:205], v[210:213], v[122:125]
	v_mfma_f32_16x16x32_bf16 v[154:157], v[178:181], v[214:217], v[154:157]
	v_mfma_f32_16x16x32_bf16 v[150:153], v[194:197], v[214:217], v[150:153]
	v_mfma_f32_16x16x32_bf16 v[130:133], v[198:201], v[214:217], v[130:133]
	s_or_b32 s23, s22, 0xc000
	v_mfma_f32_16x16x32_bf16 v[106:109], v[202:205], v[214:217], v[106:109]
	v_mfma_f32_16x16x32_bf16 v[138:141], v[178:181], v[218:221], v[138:141]
	v_mfma_f32_16x16x32_bf16 v[134:137], v[194:197], v[218:221], v[134:137]
	v_mfma_f32_16x16x32_bf16 v[114:117], v[198:201], v[218:221], v[114:117]
	s_or_b32 s23, s22, 0x10000
	v_mfma_f32_16x16x32_bf16 v[90:93], v[202:205], v[218:221], v[90:93]
	v_mfma_f32_16x16x32_bf16 v[126:129], v[178:181], v[222:225], v[126:129]
	v_mfma_f32_16x16x32_bf16 v[118:121], v[194:197], v[222:225], v[118:121]
	v_mfma_f32_16x16x32_bf16 v[98:101], v[198:201], v[222:225], v[98:101]
	s_or_b32 s23, s22, 0x14000
	v_mfma_f32_16x16x32_bf16 v[74:77], v[202:205], v[222:225], v[74:77]
	v_mfma_f32_16x16x32_bf16 v[110:113], v[178:181], v[226:229], v[110:113]
	v_mfma_f32_16x16x32_bf16 v[102:105], v[194:197], v[226:229], v[102:105]
	v_mfma_f32_16x16x32_bf16 v[82:85], v[198:201], v[226:229], v[82:85]
	s_or_b32 s23, s22, 0x18000
	s_or_b32 s22, s22, 0x1c000
	v_mfma_f32_16x16x32_bf16 v[62:65], v[202:205], v[226:229], v[62:65]
	v_mfma_f32_16x16x32_bf16 v[94:97], v[178:181], v[230:233], v[94:97]
	v_mfma_f32_16x16x32_bf16 v[86:89], v[194:197], v[230:233], v[86:89]
	v_mfma_f32_16x16x32_bf16 v[70:73], v[198:201], v[230:233], v[70:73]
	v_mfma_f32_16x16x32_bf16 v[54:57], v[202:205], v[230:233], v[54:57]
	v_mfma_f32_16x16x32_bf16 v[78:81], v[178:181], v[234:237], v[78:81]
	v_mfma_f32_16x16x32_bf16 v[66:69], v[194:197], v[234:237], v[66:69]
	v_mfma_f32_16x16x32_bf16 v[58:61], v[198:201], v[234:237], v[58:61]
	v_mfma_f32_16x16x32_bf16 v[50:53], v[202:205], v[234:237], v[50:53]
	s_waitcnt lgkmcnt(0)
	s_barrier
	ds_read_b128 v[178:181], v182 offset:33792
	ds_read_b128 v[194:197], v182 offset:35840
	ds_read_b128 v[198:201], v182 offset:37888
	ds_read_b128 v[202:205], v182 offset:39936
	ds_read_b128 v[206:209], v185 offset:1024
	ds_read_b128 v[210:213], v185 offset:3072
	ds_read_b128 v[214:217], v185 offset:5120
	ds_read_b128 v[218:221], v185 offset:7168
	ds_read_b128 v[222:225], v185 offset:9216
	ds_read_b128 v[226:229], v185 offset:11264
	ds_read_b128 v[230:233], v185 offset:13312
	ds_read_b128 v[234:237], v185 offset:15360
	s_waitcnt lgkmcnt(0)
	s_barrier
	v_mfma_f32_16x16x32_bf16 v[174:177], v[178:181], v[206:209], v[174:177]
	s_lshl_b32 s21, s21, 15
	s_and_b32 s21, s21, 0x78000
	s_or_b32 s21, s21, s14
	s_or_b32 s22, s21, 0x2000
	v_mfma_f32_16x16x32_bf16 v[170:173], v[194:197], v[206:209], v[170:173]
	v_mfma_f32_16x16x32_bf16 v[158:161], v[198:201], v[206:209], v[158:161]
	v_mfma_f32_16x16x32_bf16 v[142:145], v[202:205], v[206:209], v[142:145]
	v_mfma_f32_16x16x32_bf16 v[166:169], v[178:181], v[210:213], v[166:169]
	v_mfma_f32_16x16x32_bf16 v[162:165], v[194:197], v[210:213], v[162:165]
	v_mfma_f32_16x16x32_bf16 v[146:149], v[198:201], v[210:213], v[146:149]
	v_mfma_f32_16x16x32_bf16 v[122:125], v[202:205], v[210:213], v[122:125]
	v_mfma_f32_16x16x32_bf16 v[154:157], v[178:181], v[214:217], v[154:157]
	v_mfma_f32_16x16x32_bf16 v[150:153], v[194:197], v[214:217], v[150:153]
	v_mfma_f32_16x16x32_bf16 v[130:133], v[198:201], v[214:217], v[130:133]
	v_mfma_f32_16x16x32_bf16 v[106:109], v[202:205], v[214:217], v[106:109]
	v_mfma_f32_16x16x32_bf16 v[138:141], v[178:181], v[218:221], v[138:141]
	v_mfma_f32_16x16x32_bf16 v[134:137], v[194:197], v[218:221], v[134:137]
	s_or_b32 s22, s21, 0x4000
	s_or_b32 s21, s21, 0x6000
	v_mfma_f32_16x16x32_bf16 v[114:117], v[198:201], v[218:221], v[114:117]
	v_mfma_f32_16x16x32_bf16 v[90:93], v[202:205], v[218:221], v[90:93]
	v_mfma_f32_16x16x32_bf16 v[126:129], v[178:181], v[222:225], v[126:129]
	v_mfma_f32_16x16x32_bf16 v[118:121], v[194:197], v[222:225], v[118:121]
	v_mfma_f32_16x16x32_bf16 v[98:101], v[198:201], v[222:225], v[98:101]
	v_mfma_f32_16x16x32_bf16 v[74:77], v[202:205], v[222:225], v[74:77]
	v_mfma_f32_16x16x32_bf16 v[110:113], v[178:181], v[226:229], v[110:113]
	v_mfma_f32_16x16x32_bf16 v[102:105], v[194:197], v[226:229], v[102:105]
	v_mfma_f32_16x16x32_bf16 v[82:85], v[198:201], v[226:229], v[82:85]
	v_mfma_f32_16x16x32_bf16 v[62:65], v[202:205], v[226:229], v[62:65]
	v_mfma_f32_16x16x32_bf16 v[94:97], v[178:181], v[230:233], v[94:97]
	v_mfma_f32_16x16x32_bf16 v[86:89], v[194:197], v[230:233], v[86:89]
	v_mfma_f32_16x16x32_bf16 v[70:73], v[198:201], v[230:233], v[70:73]
	v_mfma_f32_16x16x32_bf16 v[54:57], v[202:205], v[230:233], v[54:57]
	v_mfma_f32_16x16x32_bf16 v[78:81], v[178:181], v[234:237], v[78:81]
	v_mfma_f32_16x16x32_bf16 v[66:69], v[194:197], v[234:237], v[66:69]
	v_mfma_f32_16x16x32_bf16 v[58:61], v[198:201], v[234:237], v[58:61]
	v_mfma_f32_16x16x32_bf16 v[50:53], v[202:205], v[234:237], v[50:53]
	s_and_b32 s21, s18, 32
	s_add_i32 s21, s21, s12
	s_lshl_b32 s21, s21, 6
	s_and_b32 s21, s21, 0x3f00
	v_add_lshl_u32 v182, v193, s21, 9
	v_add_u32_e32 v206, v184, v182
	buffer_store_dwordx4 v[174:177], v206, s[28:31], 0 offen
	buffer_store_dwordx4 v[170:173], v206, s[28:31], 0 offen offset:64
	buffer_store_dwordx4 v[158:161], v206, s[28:31], 0 offen offset:128
	buffer_store_dwordx4 v[142:145], v206, s[28:31], 0 offen offset:192
	buffer_store_dwordx4 v[166:169], v206, s[28:31], s8 offen
	buffer_store_dwordx4 v[162:165], v206, s[28:31], s8 offen offset:64
	buffer_store_dwordx4 v[146:149], v206, s[28:31], s8 offen offset:128
	buffer_store_dwordx4 v[122:125], v206, s[28:31], s8 offen offset:192
	buffer_store_dwordx4 v[154:157], v206, s[28:31], s15 offen
	buffer_store_dwordx4 v[150:153], v206, s[28:31], s15 offen offset:64
	buffer_store_dwordx4 v[130:133], v206, s[28:31], s15 offen offset:128
	buffer_store_dwordx4 v[106:109], v206, s[28:31], s15 offen offset:192
	buffer_store_dwordx4 v[138:141], v206, s[28:31], s9 offen
	buffer_store_dwordx4 v[134:137], v206, s[28:31], s9 offen offset:64
	buffer_store_dwordx4 v[114:117], v206, s[28:31], s9 offen offset:128
	buffer_store_dwordx4 v[90:93], v206, s[28:31], s9 offen offset:192
	buffer_store_dwordx4 v[126:129], v206, s[28:31], s16 offen
	buffer_store_dwordx4 v[118:121], v206, s[28:31], s16 offen offset:64
	buffer_store_dwordx4 v[98:101], v206, s[28:31], s16 offen offset:128
	buffer_store_dwordx4 v[74:77], v206, s[28:31], s16 offen offset:192
	buffer_store_dwordx4 v[110:113], v206, s[28:31], s10 offen
	buffer_store_dwordx4 v[102:105], v206, s[28:31], s10 offen offset:64
	buffer_store_dwordx4 v[82:85], v206, s[28:31], s10 offen offset:128
	buffer_store_dwordx4 v[62:65], v206, s[28:31], s10 offen offset:192
	buffer_store_dwordx4 v[94:97], v206, s[28:31], s17 offen
	buffer_store_dwordx4 v[86:89], v206, s[28:31], s17 offen offset:64
	buffer_store_dwordx4 v[70:73], v206, s[28:31], s17 offen offset:128
	buffer_store_dwordx4 v[54:57], v206, s[28:31], s17 offen offset:192
	buffer_store_dwordx4 v[78:81], v206, s[28:31], s11 offen
	buffer_store_dwordx4 v[66:69], v206, s[28:31], s11 offen offset:64
	buffer_store_dwordx4 v[58:61], v206, s[28:31], s11 offen offset:128
	buffer_store_dwordx4 v[50:53], v206, s[28:31], s11 offen offset:192
	s_waitcnt lgkmcnt(0)
	s_barrier
	s_branch .LBB1_6
.Lfirst:
	v_add_u32_e32 v182, s19, v191
	v_add_u32_e32 v238, s19, v192
	v_xor_b32_e32 v185, 64, v238
	ds_read_b128 v[178:181], v182 offset:32768
	ds_read_b128 v[194:197], v182 offset:34816
	ds_read_b128 v[198:201], v182 offset:36864
	ds_read_b128 v[202:205], v182 offset:38912
	ds_read_b128 v[206:209], v238
	ds_read_b128 v[210:213], v238 offset:2048
	ds_read_b128 v[214:217], v238 offset:4096
	ds_read_b128 v[218:221], v238 offset:6144
	ds_read_b128 v[222:225], v238 offset:8192
	ds_read_b128 v[226:229], v238 offset:10240
	ds_read_b128 v[230:233], v238 offset:12288
	ds_read_b128 v[234:237], v238 offset:14336
	s_min_u32 s21, s20, 29
	s_xor_b32 s19, s19, 0x10000
	v_add_u32_e32 v239, s19, v189
	s_waitcnt vmcnt(11)
	v_cvt_pk_bf16_f32 v13, v12, v13
	v_cvt_pk_bf16_f32 v12, v10, v11
	s_waitcnt vmcnt(10)
	v_cvt_pk_bf16_f32 v11, v20, v21
	v_cvt_pk_bf16_f32 v10, v18, v19
	ds_write2st64_b64 v239, v[12:13], v[10:11] offset1:8
	s_waitcnt vmcnt(9)
	v_cvt_pk_bf16_f32 v11, v24, v25
	v_cvt_pk_bf16_f32 v10, v22, v23
	s_waitcnt vmcnt(8)
	v_cvt_pk_bf16_f32 v13, v32, v33
	v_cvt_pk_bf16_f32 v12, v30, v31
	ds_write2st64_b64 v239, v[10:11], v[12:13] offset0:16 offset1:24
	s_waitcnt vmcnt(7)
	v_cvt_pk_bf16_f32 v11, v36, v37
	v_cvt_pk_bf16_f32 v10, v34, v35
	s_waitcnt vmcnt(6)
	v_cvt_pk_bf16_f32 v13, v40, v41
	v_cvt_pk_bf16_f32 v12, v38, v39
	ds_write2st64_b64 v239, v[10:11], v[12:13] offset0:32 offset1:40
	s_waitcnt vmcnt(5)
	v_cvt_pk_bf16_f32 v11, v44, v45
	v_cvt_pk_bf16_f32 v10, v42, v43
	s_waitcnt vmcnt(4)
	v_cvt_pk_bf16_f32 v13, v48, v49
	v_cvt_pk_bf16_f32 v12, v46, v47
	ds_write2st64_b64 v239, v[10:11], v[12:13] offset0:48 offset1:56
	s_waitcnt lgkmcnt(0)
	s_add_i32 s21, s21, 2
	s_barrier
	v_mfma_f32_16x16x32_bf16 v[174:177], v[178:181], v[206:209], v[240:243]
	s_lshl_b32 s22, s21, 1
	s_and_b32 s22, s22, 0x60
	s_add_i32 s22, s22, s12
	s_lshl_b32 s22, s22, 6
	v_mfma_f32_16x16x32_bf16 v[170:173], v[194:197], v[206:209], v[244:247]
	s_and_b32 s22, s22, 0x3f00
	s_or_b32 s22, s22, s13
	s_lshl_b32 s23, s21, 23
	s_lshl_b32 s22, s22, 9
	v_mfma_f32_16x16x32_bf16 v[158:161], v[198:201], v[206:209], v[248:251]
	s_and_b32 s23, s23, 0x7000000
	s_or_b32 s22, s22, s23
	s_lshl_b32 s23, s21, 8
	s_and_b32 s23, s23, 0x100
	s_or_b32 s22, s22, s23
	s_or_b32 s23, s22, 0x4000
	buffer_load_dwordx4 v[10:13], v1, s[4:7], s22 offen sc0 nt
	v_mfma_f32_16x16x32_bf16 v[142:145], v[202:205], v[206:209], v[252:255]
	v_mfma_f32_16x16x32_bf16 v[166:169], v[178:181], v[210:213], v[240:243]
	v_mfma_f32_16x16x32_bf16 v[162:165], v[194:197], v[210:213], v[244:247]
	v_mfma_f32_16x16x32_bf16 v[146:149], v[198:201], v[210:213], v[248:251]
	buffer_load_dwordx4 v[18:21], v1, s[4:7], s23 offen sc0 nt
	s_or_b32 s23, s22, 0x8000
	v_mfma_f32_16x16x32_bf16 v[122:125], v[202:205], v[210:213], v[252:255]
	v_mfma_f32_16x16x32_bf16 v[154:157], v[178:181], v[214:217], v[240:243]
	v_mfma_f32_16x16x32_bf16 v[150:153], v[194:197], v[214:217], v[244:247]
	v_mfma_f32_16x16x32_bf16 v[130:133], v[198:201], v[214:217], v[248:251]
	buffer_load_dwordx4 v[22:25], v1, s[4:7], s23 offen sc0 nt
	s_or_b32 s23, s22, 0xc000
	v_mfma_f32_16x16x32_bf16 v[106:109], v[202:205], v[214:217], v[252:255]
	v_mfma_f32_16x16x32_bf16 v[138:141], v[178:181], v[218:221], v[240:243]
	v_mfma_f32_16x16x32_bf16 v[134:137], v[194:197], v[218:221], v[244:247]
	v_mfma_f32_16x16x32_bf16 v[114:117], v[198:201], v[218:221], v[248:251]
	buffer_load_dwordx4 v[30:33], v1, s[4:7], s23 offen sc0 nt
	s_or_b32 s23, s22, 0x10000
	v_mfma_f32_16x16x32_bf16 v[90:93], v[202:205], v[218:221], v[252:255]
	v_mfma_f32_16x16x32_bf16 v[126:129], v[178:181], v[222:225], v[240:243]
	v_mfma_f32_16x16x32_bf16 v[118:121], v[194:197], v[222:225], v[244:247]
	v_mfma_f32_16x16x32_bf16 v[98:101], v[198:201], v[222:225], v[248:251]
	buffer_load_dwordx4 v[34:37], v1, s[4:7], s23 offen sc0 nt
	s_or_b32 s23, s22, 0x14000
	v_mfma_f32_16x16x32_bf16 v[74:77], v[202:205], v[222:225], v[252:255]
	v_mfma_f32_16x16x32_bf16 v[110:113], v[178:181], v[226:229], v[240:243]
	v_mfma_f32_16x16x32_bf16 v[102:105], v[194:197], v[226:229], v[244:247]
	v_mfma_f32_16x16x32_bf16 v[82:85], v[198:201], v[226:229], v[248:251]
	buffer_load_dwordx4 v[38:41], v1, s[4:7], s23 offen sc0 nt
	s_or_b32 s23, s22, 0x18000
	s_or_b32 s22, s22, 0x1c000
	v_mfma_f32_16x16x32_bf16 v[62:65], v[202:205], v[226:229], v[252:255]
	v_mfma_f32_16x16x32_bf16 v[94:97], v[178:181], v[230:233], v[240:243]
	v_mfma_f32_16x16x32_bf16 v[86:89], v[194:197], v[230:233], v[244:247]
	v_mfma_f32_16x16x32_bf16 v[70:73], v[198:201], v[230:233], v[248:251]
	buffer_load_dwordx4 v[42:45], v1, s[4:7], s23 offen sc0 nt
	v_mfma_f32_16x16x32_bf16 v[54:57], v[202:205], v[230:233], v[252:255]
	v_mfma_f32_16x16x32_bf16 v[78:81], v[178:181], v[234:237], v[240:243]
	v_mfma_f32_16x16x32_bf16 v[66:69], v[194:197], v[234:237], v[244:247]
	v_mfma_f32_16x16x32_bf16 v[58:61], v[198:201], v[234:237], v[248:251]
	buffer_load_dwordx4 v[46:49], v1, s[4:7], s22 offen sc0 nt
	v_mfma_f32_16x16x32_bf16 v[50:53], v[202:205], v[234:237], v[252:255]
	s_waitcnt lgkmcnt(0)
	s_barrier
	ds_read_b128 v[178:181], v182 offset:33792
	ds_read_b128 v[194:197], v182 offset:35840
	ds_read_b128 v[198:201], v182 offset:37888
	ds_read_b128 v[202:205], v182 offset:39936
	ds_read_b128 v[206:209], v185 offset:1024
	ds_read_b128 v[210:213], v185 offset:3072
	ds_read_b128 v[214:217], v185 offset:5120
	ds_read_b128 v[218:221], v185 offset:7168
	ds_read_b128 v[222:225], v185 offset:9216
	ds_read_b128 v[226:229], v185 offset:11264
	ds_read_b128 v[230:233], v185 offset:13312
	ds_read_b128 v[234:237], v185 offset:15360
	v_add_u32_e32 v182, s19, v190
	s_waitcnt vmcnt(11)
	ds_write_b128 v182, v[2:5] offset:32768
	s_waitcnt vmcnt(10)
	ds_write_b128 v182, v[6:9] offset:40960
	s_waitcnt vmcnt(9)
	ds_write_b128 v182, v[14:17] offset:49152
	s_waitcnt vmcnt(8)
	ds_write_b128 v182, v[26:29] offset:57344
	s_waitcnt lgkmcnt(0)
	s_barrier
	v_mfma_f32_16x16x32_bf16 v[174:177], v[178:181], v[206:209], v[174:177]
	s_lshl_b32 s21, s21, 15
	s_and_b32 s21, s21, 0x78000
	s_or_b32 s21, s21, s14
	s_or_b32 s22, s21, 0x2000
	v_mfma_f32_16x16x32_bf16 v[170:173], v[194:197], v[206:209], v[170:173]
	v_mfma_f32_16x16x32_bf16 v[158:161], v[198:201], v[206:209], v[158:161]
	v_mfma_f32_16x16x32_bf16 v[142:145], v[202:205], v[206:209], v[142:145]
	v_mfma_f32_16x16x32_bf16 v[166:169], v[178:181], v[210:213], v[166:169]
	v_mfma_f32_16x16x32_bf16 v[162:165], v[194:197], v[210:213], v[162:165]
	buffer_load_dwordx4 v[2:5], v188, s[0:3], s21 offen sc1
	v_mfma_f32_16x16x32_bf16 v[146:149], v[198:201], v[210:213], v[146:149]
	v_mfma_f32_16x16x32_bf16 v[122:125], v[202:205], v[210:213], v[122:125]
	v_mfma_f32_16x16x32_bf16 v[154:157], v[178:181], v[214:217], v[154:157]
	v_mfma_f32_16x16x32_bf16 v[150:153], v[194:197], v[214:217], v[150:153]
	v_mfma_f32_16x16x32_bf16 v[130:133], v[198:201], v[214:217], v[130:133]
	v_mfma_f32_16x16x32_bf16 v[106:109], v[202:205], v[214:217], v[106:109]
	v_mfma_f32_16x16x32_bf16 v[138:141], v[178:181], v[218:221], v[138:141]
	v_mfma_f32_16x16x32_bf16 v[134:137], v[194:197], v[218:221], v[134:137]
	buffer_load_dwordx4 v[6:9], v188, s[0:3], s22 offen sc1
	s_or_b32 s22, s21, 0x4000
	s_or_b32 s21, s21, 0x6000
	v_mfma_f32_16x16x32_bf16 v[114:117], v[198:201], v[218:221], v[114:117]
	v_mfma_f32_16x16x32_bf16 v[90:93], v[202:205], v[218:221], v[90:93]
	v_mfma_f32_16x16x32_bf16 v[126:129], v[178:181], v[222:225], v[126:129]
	v_mfma_f32_16x16x32_bf16 v[118:121], v[194:197], v[222:225], v[118:121]
	v_mfma_f32_16x16x32_bf16 v[98:101], v[198:201], v[222:225], v[98:101]
	v_mfma_f32_16x16x32_bf16 v[74:77], v[202:205], v[222:225], v[74:77]
	v_mfma_f32_16x16x32_bf16 v[110:113], v[178:181], v[226:229], v[110:113]
	v_mfma_f32_16x16x32_bf16 v[102:105], v[194:197], v[226:229], v[102:105]
	buffer_load_dwordx4 v[14:17], v188, s[0:3], s22 offen sc1
	v_mfma_f32_16x16x32_bf16 v[82:85], v[198:201], v[226:229], v[82:85]
	v_mfma_f32_16x16x32_bf16 v[62:65], v[202:205], v[226:229], v[62:65]
	v_mfma_f32_16x16x32_bf16 v[94:97], v[178:181], v[230:233], v[94:97]
	v_mfma_f32_16x16x32_bf16 v[86:89], v[194:197], v[230:233], v[86:89]
	v_mfma_f32_16x16x32_bf16 v[70:73], v[198:201], v[230:233], v[70:73]
	v_mfma_f32_16x16x32_bf16 v[54:57], v[202:205], v[230:233], v[54:57]
	v_mfma_f32_16x16x32_bf16 v[78:81], v[178:181], v[234:237], v[78:81]
	v_mfma_f32_16x16x32_bf16 v[66:69], v[194:197], v[234:237], v[66:69]
	buffer_load_dwordx4 v[26:29], v188, s[0:3], s21 offen sc1
	v_mfma_f32_16x16x32_bf16 v[58:61], v[198:201], v[234:237], v[58:61]
	v_mfma_f32_16x16x32_bf16 v[50:53], v[202:205], v[234:237], v[50:53]
	s_branch .LBB1_3
